# grid barrier: TOP counter removed - each XCD leader adds 1 to every XGEN word after its write-back, all wait for XGEN >= (gen+1)*nx; MoE prologue n_mt/mt_e loads merged; P15 row-scale loads at unit he
# baseline (speedup 1.0000x reference)
.Lxb0_poll:
	s_waitcnt lgkmcnt(0)
	v_add_u32_e32 v6, 1, v2
	v_mul_lo_u32 v6, v6, v1
	s_mov_b32 s10, 0
	v_mov_b32_e32 v4, 0x2000
.Lxb0_spin:
	global_load_dword v5, v4, s[4:5] offset:1024 sc1
	s_waitcnt vmcnt(0)
	v_cmp_ge_u32_e32 vcc, v5, v6
	s_cbranch_vccnz .Lxb0_acq
	s_sleep 1
	s_add_u32 s10, s10, 1
	s_cmp_lt_u32 s10, 0x10000
	s_cbranch_scc1 .Lxb0_spin
	s_branch .Lxb0_acq
.Lxb0_lead:
	buffer_wbl2 sc1
	v_readlane_b32 s8, v254, 40
	v_readlane_b32 s9, v254, 41
	v_mov_b32_e32 v4, 0x2400
	v_mov_b32_e32 v5, 1
	s_nop 3
	s_waitcnt vmcnt(0)
	global_atomic_add v4, v5, s[8:9]
	global_atomic_add v4, v5, s[8:9] offset:256
	global_atomic_add v4, v5, s[8:9] offset:512
	global_atomic_add v4, v5, s[8:9] offset:768
	global_atomic_add v4, v5, s[8:9] offset:1024
	global_atomic_add v4, v5, s[8:9] offset:1280
	global_atomic_add v4, v5, s[8:9] offset:1536
	global_atomic_add v4, v5, s[8:9] offset:1792
	global_atomic_add v4, v5, s[8:9] offset:2048
	global_atomic_add v4, v5, s[8:9] offset:2304
	global_atomic_add v4, v5, s[8:9] offset:2560
	global_atomic_add v4, v5, s[8:9] offset:2816
	global_atomic_add v4, v5, s[8:9] offset:3072
	global_atomic_add v4, v5, s[8:9] offset:3328
	global_atomic_add v4, v5, s[8:9] offset:3584
	global_atomic_add v4, v5, s[8:9] offset:3840
	s_branch .Lxb0_poll

.Lxb1_spin:
	global_load_dword v5, v4, s[2:3] offset:1024 sc1
	s_waitcnt vmcnt(0)
	v_cmp_ge_u32_e32 vcc, v5, v6
	s_cbranch_vccnz .Lxb1_acq
	s_sleep 1
	s_add_u32 s10, s10, 1
	s_cmp_lt_u32 s10, 0x10000
	s_cbranch_scc1 .Lxb1_spin
	s_branch .Lxb1_acq

.LBB0_3815:
	s_cmp_lt_i32 s56, 16
	s_cselect_b64 s[0:1], -1, 0
	s_cmp_gt_i32 s57, 15
	s_cselect_b64 s[4:5], -1, 0
	s_and_b64 s[0:1], s[0:1], s[4:5]
	s_andn2_b64 vcc, exec, s[0:1]
	s_cbranch_vccnz .LBB0_3897
	s_waitcnt vmcnt(0)
	v_mov_b32_e32 v4, v0
	v_mov_b32_e32 v1, 0
	global_load_dword v16, v1, s[2:3] sc1
	s_movk_i32 s0, 0x88
	v_cmp_gt_i32_e32 vcc, s0, v4
	s_and_saveexec_b64 s[0:1], vcc
	s_cbranch_execz .LBB0_3819
	v_ashrrev_i32_e32 v5, 31, v4
	v_add_u32_e32 v1, 0xfffffe00, v4
	v_lshl_add_u64 v[2:3], v[4:5], 2, s[96:97]
	s_mov_b64 s[4:5], 0x504000
	v_lshl_add_u32 v4, v4, 2, 0
	v_lshl_add_u64 v[2:3], v[2:3], 0, s[4:5]
	v_add_u32_e32 v4, 0x20000, v4
	s_mov_b64 s[4:5], 0
	s_mov_b64 s[8:9], 0x800
	s_movk_i32 s10, 0xfe87

.LBB0_3819:
	s_or_b64 exec, exec, s[0:1]
	s_waitcnt vmcnt(0)
	v_readfirstlane_b32 s38, v16
	v_mov_b32_e32 v2, 0x508000
	s_waitcnt lgkmcnt(0)
	s_barrier
	global_load_dword v1, v2, s[96:97] offset:16 sc1
	global_load_dword v8, v2, s[96:97] offset:20 sc1
	s_mul_i32 s0, s38, 56
	s_cmp_ge_i32 s86, s0
	v_readfirstlane_b32 s1, v0
	s_cbranch_scc1 .LBB0_3847
	v_and_b32_e32 v2, 32, v0
	s_add_u32 s39, s96, 0x3ea00000
	v_bitop3_b32 v6, v249, v2, 48 bitop3:0x6c
	v_and_b32_e32 v2, 64, v0
	s_addc_u32 s40, s97, 0
	v_or_b32_e32 v2, v6, v2
	v_lshrrev_b32_e32 v4, 5, v0
	s_add_u32 s41, s96, 0x8a00000
	v_lshlrev_b32_e32 v3, 8, v2
	s_movk_i32 s8, 0x6010
	v_and_b32_e32 v4, 4, v4
	v_and_b32_e32 v194, 24, v226
	v_bfe_u32 v5, v0, 2, 2
	v_or_b32_e32 v7, 0x2000, v249
	s_addc_u32 s42, s97, 0
	v_bitop3_b32 v3, v3, s8, v249 bitop3:0xc8
	v_or3_b32 v4, v4, v5, v194
	v_lshrrev_b32_e32 v5, 7, v7
	s_movk_i32 s8, 0x60
	s_ashr_i32 s45, s86, 31
	v_and_or_b32 v9, v5, s8, v4
	s_lshr_b32 s8, s45, 29
	s_add_i32 s8, s86, s8
	s_and_b32 s9, s8, -8
	s_sub_i32 s9, s86, s9
	s_mul_i32 s44, s38, 7
	s_lshr_b32 s10, s9, 31
	s_add_i32 s10, s44, s10
	s_mul_i32 s9, s10, s9
	s_ashr_i32 s8, s8, 3
	s_add_i32 s9, s9, s8
	s_mul_hi_i32 s8, s9, 0x92492493
	s_add_i32 s8, s8, s9
	s_lshr_b32 s10, s8, 31
	s_ashr_i32 s8, s8, 7
	s_add_i32 s8, s8, s10
	s_lshl_b32 s10, s8, 2
	s_sub_i32 s11, s38, s10
	s_min_i32 s11, s11, 4
	s_abs_i32 s12, s11
	v_lshl_or_b32 v196, v9, 5, v3
	v_cvt_f32_u32_e32 v9, s12
	s_movk_i32 s13, 0x70
	v_bfe_u32 v10, v0, 2, 4
	v_and_or_b32 v5, v5, s13, v10
	v_lshl_or_b32 v198, v5, 11, v2
	v_rcp_iflag_f32_e32 v5, v9
	s_sub_i32 s14, 0, s12
	s_mulk_i32 s8, 0xe0
	s_sub_i32 s8, s9, s8
	v_mul_f32_e32 v5, 0x4f7ffffe, v5
	v_cvt_u32_f32_e32 v5, v5
	s_abs_i32 s13, s8
	s_lshr_b32 s5, s1, 6
	s_xor_b32 s9, s8, s11
	v_readfirstlane_b32 s15, v5
	s_mul_i32 s14, s14, s15
	s_mul_hi_u32 s14, s15, s14
	s_add_i32 s15, s15, s14
	s_mul_hi_u32 s14, s13, s15
	s_mul_i32 s15, s14, s12
	s_sub_i32 s13, s13, s15
	s_lshr_b32 s4, s1, 8
	s_lshl_b32 s43, s5, 10
	s_ashr_i32 s9, s9, 31
	s_add_i32 s15, s14, 1
	s_sub_i32 s16, s13, s12
	s_cmp_ge_u32 s13, s12
	s_cselect_b32 s14, s15, s14
	s_cselect_b32 s13, s16, s13
	s_add_i32 s15, s14, 1
	s_cmp_ge_u32 s13, s12
	s_cselect_b32 s12, s15, s14
	s_xor_b32 s12, s12, s9
	s_sub_i32 s24, s12, s9
	s_mul_i32 s9, s24, s11
	s_sub_i32 s8, s8, s9
	s_add_i32 s22, s10, s8
	s_lshl_b32 s8, s22, 2
	s_add_i32 s8, s8, 0
	s_add_i32 s8, s8, 0x20000
	v_mov_b32_e32 v5, s8
	ds_read_b32 v5, v5
	s_ashr_i32 s23, s22, 31
	v_lshrrev_b32_e32 v9, 3, v0
	v_and_or_b32 v4, v9, 32, v4
	v_lshl_or_b32 v200, v4, 5, v3
	s_waitcnt lgkmcnt(0)
	v_readfirstlane_b32 s8, v5
	s_mul_hi_i32 s10, s8, 0x1c00000
	s_mul_i32 s11, s8, 0x1c00000
	s_lshl_b64 s[8:9], s[22:23], 19
	s_add_u32 s12, s41, s11
	s_addc_u32 s13, s42, s10
	s_ashr_i32 s25, s24, 31
	s_lshl_b64 s[10:11], s[24:25], 19
	s_add_u32 s28, s12, s10
	s_addc_u32 s29, s13, s11
	s_add_i32 s23, s43, 0
	s_add_i32 s25, s23, 0x10000
	s_add_i32 s46, s23, 0x12000
	s_mov_b32 m0, s25
	s_add_u32 s10, s28, 0x1000
	global_load_lds_dwordx4 v200, s[28:29]
	s_mov_b32 m0, s46
	s_addc_u32 s11, s29, 0
	s_add_i32 s47, s23, 0x14000
	s_add_i32 s51, s23, 0x16000
	global_load_lds_dwordx4 v196, s[28:29]
	s_mov_b32 m0, s47
	s_add_u32 s26, s39, s8
	v_and_or_b32 v3, v9, 48, v10
	global_load_lds_dwordx4 v200, s[10:11]
	s_mov_b32 m0, s51
	s_addc_u32 s27, s40, s9
	s_add_i32 s52, s23, 0x2000
	v_lshl_or_b32 v202, v3, 11, v2
	global_load_lds_dwordx4 v196, s[10:11]
	s_mov_b32 m0, s23
	s_add_u32 s8, s26, 0x40000
	global_load_lds_dwordx4 v202, s[26:27]
	s_mov_b32 m0, s52
	s_addc_u32 s9, s27, 0
	s_add_i32 s53, s23, 0x4000
	global_load_lds_dwordx4 v198, s[26:27]
	s_mov_b32 m0, s53
	s_add_i32 s54, s23, 0x6000
	global_load_lds_dwordx4 v202, s[8:9]
	s_mov_b32 m0, s54
	v_mov_b32_e32 v201, 0
	global_load_lds_dwordx4 v198, s[8:9]
	v_mov_b32_e32 v203, v201
	v_mov_b32_e32 v199, v201
	s_cmp_eq_u32 s4, 1
	s_mov_b32 s30, 0
	v_mov_b32_e32 v197, v201
	v_lshl_add_u64 v[2:3], s[26:27], 0, v[202:203]
	s_cselect_b64 s[8:9], -1, 0
	s_cmp_lg_u32 s4, 1
	v_lshl_add_u64 v[4:5], s[26:27], 0, v[198:199]
	s_cbranch_scc1 .LBB0_3822
	s_barrier

.LBB0_3829:
	s_ashr_i32 s17, s16, 31
	s_lshl_b64 s[20:21], s[16:17], 19
	s_add_u32 s20, s39, s20
	s_addc_u32 s21, s40, s21
	s_and_b64 s[4:5], s[4:5], exec
	s_cselect_b32 s15, s21, s27
	s_cselect_b32 s17, s20, s26
	s_cmp_eq_u32 s30, 0
	s_cselect_b32 s67, -2, 0
	s_add_u32 s69, s28, 0x10000
	s_mov_b32 s68, 0
	s_addc_u32 s70, s29, 0
	v_lshl_add_u64 v[238:239], s[26:27], 0, v[216:217]
	v_lshl_add_u64 v[240:241], s[26:27], 0, v[218:219]
	s_mov_b64 s[4:5], 0
	v_mov_b32_e32 v2, 0
	v_mov_b32_e32 v3, 0
	v_mov_b32_e32 v4, 0
	v_mov_b32_e32 v5, 0
	v_mov_b32_e32 v6, 0
	v_mov_b32_e32 v7, 0
	v_mov_b32_e32 v8, 0
	v_mov_b32_e32 v9, 0
	v_mov_b32_e32 v18, 0
	v_mov_b32_e32 v19, 0
	v_mov_b32_e32 v20, 0
	v_mov_b32_e32 v21, 0
	v_mov_b32_e32 v22, 0
	v_mov_b32_e32 v23, 0
	v_mov_b32_e32 v24, 0
	v_mov_b32_e32 v25, 0
	v_mov_b32_e32 v34, 0
	v_mov_b32_e32 v35, 0
	v_mov_b32_e32 v36, 0
	v_mov_b32_e32 v37, 0
	v_mov_b32_e32 v38, 0
	v_mov_b32_e32 v39, 0
	v_mov_b32_e32 v40, 0
	v_mov_b32_e32 v41, 0
	v_mov_b32_e32 v50, 0
	v_mov_b32_e32 v51, 0
	v_mov_b32_e32 v52, 0
	v_mov_b32_e32 v53, 0
	v_mov_b32_e32 v54, 0
	v_mov_b32_e32 v55, 0
	v_mov_b32_e32 v56, 0
	v_mov_b32_e32 v57, 0
	v_mov_b32_e32 v10, 0
	v_mov_b32_e32 v11, 0
	v_mov_b32_e32 v12, 0
	v_mov_b32_e32 v13, 0
	v_mov_b32_e32 v14, 0
	v_mov_b32_e32 v15, 0
	v_mov_b32_e32 v16, 0
	v_mov_b32_e32 v17, 0
	v_mov_b32_e32 v26, 0
	v_mov_b32_e32 v27, 0
	v_mov_b32_e32 v28, 0
	v_mov_b32_e32 v29, 0
	v_mov_b32_e32 v30, 0
	v_mov_b32_e32 v31, 0
	v_mov_b32_e32 v32, 0
	v_mov_b32_e32 v33, 0
	v_mov_b32_e32 v42, 0
	v_mov_b32_e32 v43, 0
	v_mov_b32_e32 v44, 0
	v_mov_b32_e32 v45, 0
	v_mov_b32_e32 v46, 0
	v_mov_b32_e32 v47, 0
	v_mov_b32_e32 v48, 0
	v_mov_b32_e32 v49, 0
	v_mov_b32_e32 v58, 0
	v_mov_b32_e32 v59, 0
	v_mov_b32_e32 v60, 0
	v_mov_b32_e32 v61, 0
	v_mov_b32_e32 v62, 0
	v_mov_b32_e32 v63, 0
	v_mov_b32_e32 v64, 0
	v_mov_b32_e32 v65, 0
	v_mov_b32_e32 v66, 0
	v_mov_b32_e32 v67, 0
	v_mov_b32_e32 v68, 0
	v_mov_b32_e32 v69, 0
	v_mov_b32_e32 v70, 0
	v_mov_b32_e32 v71, 0
	v_mov_b32_e32 v72, 0
	v_mov_b32_e32 v73, 0
	v_mov_b32_e32 v82, 0
	v_mov_b32_e32 v83, 0
	v_mov_b32_e32 v84, 0
	v_mov_b32_e32 v85, 0
	v_mov_b32_e32 v86, 0
	v_mov_b32_e32 v87, 0
	v_mov_b32_e32 v88, 0
	v_mov_b32_e32 v89, 0
	v_mov_b32_e32 v98, 0
	v_mov_b32_e32 v99, 0
	v_mov_b32_e32 v100, 0
	v_mov_b32_e32 v101, 0
	v_mov_b32_e32 v102, 0
	v_mov_b32_e32 v103, 0
	v_mov_b32_e32 v104, 0
	v_mov_b32_e32 v105, 0
	v_mov_b32_e32 v114, 0
	v_mov_b32_e32 v115, 0
	v_mov_b32_e32 v116, 0
	v_mov_b32_e32 v117, 0
	v_mov_b32_e32 v118, 0
	v_mov_b32_e32 v119, 0
	v_mov_b32_e32 v120, 0
	v_mov_b32_e32 v121, 0
	v_mov_b32_e32 v74, 0
	v_mov_b32_e32 v75, 0
	v_mov_b32_e32 v76, 0
	v_mov_b32_e32 v77, 0
	v_mov_b32_e32 v78, 0
	v_mov_b32_e32 v79, 0
	v_mov_b32_e32 v80, 0
	v_mov_b32_e32 v81, 0
	v_mov_b32_e32 v90, 0
	v_mov_b32_e32 v91, 0
	v_mov_b32_e32 v92, 0
	v_mov_b32_e32 v93, 0
	v_mov_b32_e32 v94, 0
	v_mov_b32_e32 v95, 0
	v_mov_b32_e32 v96, 0
	v_mov_b32_e32 v97, 0
	v_mov_b32_e32 v106, 0
	v_mov_b32_e32 v107, 0
	v_mov_b32_e32 v108, 0
	v_mov_b32_e32 v109, 0
	v_mov_b32_e32 v110, 0
	v_mov_b32_e32 v111, 0
	v_mov_b32_e32 v112, 0
	v_mov_b32_e32 v113, 0
	v_mov_b32_e32 v122, 0
	v_mov_b32_e32 v123, 0
	v_mov_b32_e32 v124, 0
	v_mov_b32_e32 v125, 0
	v_mov_b32_e32 v126, 0
	v_mov_b32_e32 v127, 0
	v_mov_b32_e32 v128, 0
	v_mov_b32_e32 v129, 0
	s_cmp_eq_u32 s22, s64
	s_cbranch_scc1 .Lp15_rs
	v_lshl_add_u32 v130, s22, 8, v1
	v_readlane_b32 s98, v254, 47
	v_ashrrev_i32_e32 v131, 31, v130
	v_readlane_b32 s99, v254, 48
	s_mov_b32 s64, s22
	s_nop 0
	v_lshl_add_u64 v[130:131], v[130:131], 2, s[98:99]
	global_load_dword v236, v[130:131], off offset:704
	global_load_dword v234, v[130:131], off offset:640
	global_load_dword v232, v[130:131], off offset:576
	global_load_dword v230, v[130:131], off offset:512
	global_load_dword v228, v[130:131], off offset:192
	global_load_dword v226, v[130:131], off offset:128
	global_load_dword v224, v[130:131], off offset:64
	global_load_dword v222, v[130:131], off
.Lp15_rs:
	s_branch .LBB0_3831
.LBB0_3830:
	s_waitcnt lgkmcnt(0)
	s_add_i32 s36, s68, 2
	s_add_u32 s34, s28, 0x8000
	s_addc_u32 s35, s29, 0
	s_barrier
	s_setprio 1
	s_waitcnt lgkmcnt(0)
	v_mfma_i32_16x16x64_i8 v[62:65], v[146:149], v[186:189], v[62:65]
	v_mfma_i32_16x16x64_i8 v[58:61], v[150:153], v[186:189], v[58:61]
	v_mfma_i32_16x16x64_i8 v[46:49], v[146:149], v[178:181], v[46:49]
	v_mfma_i32_16x16x64_i8 v[42:45], v[150:153], v[178:181], v[42:45]
	v_mfma_i32_16x16x64_i8 v[30:33], v[146:149], v[170:173], v[30:33]
	v_mfma_i32_16x16x64_i8 v[26:29], v[150:153], v[170:173], v[26:29]
	v_mfma_i32_16x16x64_i8 v[14:17], v[146:149], v[162:165], v[14:17]
	v_mfma_i32_16x16x64_i8 v[10:13], v[150:153], v[162:165], v[10:13]
	v_mfma_i32_16x16x64_i8 v[62:65], v[158:161], v[190:193], v[62:65]
	v_mfma_i32_16x16x64_i8 v[58:61], v[154:157], v[190:193], v[58:61]
	v_mfma_i32_16x16x64_i8 v[46:49], v[158:161], v[182:185], v[46:49]
	v_mfma_i32_16x16x64_i8 v[42:45], v[154:157], v[182:185], v[42:45]
	v_mfma_i32_16x16x64_i8 v[30:33], v[158:161], v[174:177], v[30:33]
	v_mfma_i32_16x16x64_i8 v[26:29], v[154:157], v[174:177], v[26:29]
	v_mfma_i32_16x16x64_i8 v[14:17], v[158:161], v[166:169], v[14:17]
	v_mfma_i32_16x16x64_i8 v[10:13], v[154:157], v[166:169], v[10:13]
	s_setprio 0
	s_setprio 1
	v_mfma_i32_16x16x64_i8 v[54:57], v[130:133], v[186:189], v[54:57]
	v_mfma_i32_16x16x64_i8 v[50:53], v[134:137], v[186:189], v[50:53]
	v_mfma_i32_16x16x64_i8 v[38:41], v[130:133], v[178:181], v[38:41]
	v_mfma_i32_16x16x64_i8 v[34:37], v[134:137], v[178:181], v[34:37]
	v_mfma_i32_16x16x64_i8 v[22:25], v[130:133], v[170:173], v[22:25]
	v_mfma_i32_16x16x64_i8 v[18:21], v[134:137], v[170:173], v[18:21]
	v_mfma_i32_16x16x64_i8 v[6:9], v[130:133], v[162:165], v[6:9]
	v_mfma_i32_16x16x64_i8 v[2:5], v[134:137], v[162:165], v[2:5]
	v_mfma_i32_16x16x64_i8 v[54:57], v[142:145], v[190:193], v[54:57]
	v_mfma_i32_16x16x64_i8 v[50:53], v[138:141], v[190:193], v[50:53]
	v_mfma_i32_16x16x64_i8 v[38:41], v[142:145], v[182:185], v[38:41]
	v_mfma_i32_16x16x64_i8 v[34:37], v[138:141], v[182:185], v[34:37]
	v_mfma_i32_16x16x64_i8 v[22:25], v[142:145], v[174:177], v[22:25]
	v_mfma_i32_16x16x64_i8 v[18:21], v[138:141], v[174:177], v[18:21]
	v_mfma_i32_16x16x64_i8 v[6:9], v[142:145], v[166:169], v[6:9]
	v_mfma_i32_16x16x64_i8 v[2:5], v[138:141], v[166:169], v[2:5]
	s_setprio 0
	s_barrier
	s_add_i32 s37, 0, 0x18000
	s_add_i32 s71, 0, 0x1c000
	v_add_u32_e32 v134, s37, v229
	v_add_u32_e32 v142, s37, v231
	v_add_u32_e32 v150, s71, v229
	v_add_u32_e32 v158, s71, v231
	ds_read_b128 v[130:133], v134
	ds_read_b128 v[134:137], v134 offset:2048
	ds_read_b128 v[138:141], v142
	ds_read_b128 v[142:145], v142 offset:2048
	ds_read_b128 v[146:149], v150
	ds_read_b128 v[150:153], v150 offset:2048
	ds_read_b128 v[154:157], v158
	ds_read_b128 v[158:161], v158 offset:2048
	s_add_u32 s30, s30, 0x40000
	s_addc_u32 s31, s31, 0
	s_mov_b32 m0, s53
	v_lshl_add_u64 v[246:247], s[30:31], 0, v[202:203]
	ds_read_b128 v[162:165], v233 offset:32768
	ds_read_b128 v[166:169], v233 offset:33792
	ds_read_b128 v[170:173], v233 offset:34816
	ds_read_b128 v[174:177], v233 offset:35840
	ds_read_b128 v[178:181], v233 offset:36864
	ds_read_b128 v[182:185], v233 offset:37888
	ds_read_b128 v[186:189], v233 offset:38912
	ds_read_b128 v[190:193], v233 offset:39936
	global_load_lds_dwordx4 v[246:247], off
	v_lshl_add_u64 v[246:247], s[30:31], 0, v[198:199]
	s_mov_b32 m0, s54
	s_nop 0
	global_load_lds_dwordx4 v[246:247], off
	s_waitcnt vmcnt(8)
	s_waitcnt lgkmcnt(0)
	s_barrier
	s_setprio 1
	s_waitcnt lgkmcnt(0)
	v_mfma_i32_16x16x64_i8 v[126:129], v[130:133], v[162:165], v[126:129]
	v_mfma_i32_16x16x64_i8 v[122:125], v[134:137], v[162:165], v[122:125]
	v_mfma_i32_16x16x64_i8 v[110:113], v[130:133], v[170:173], v[110:113]
	v_mfma_i32_16x16x64_i8 v[106:109], v[134:137], v[170:173], v[106:109]
	v_mfma_i32_16x16x64_i8 v[94:97], v[130:133], v[178:181], v[94:97]
	v_mfma_i32_16x16x64_i8 v[90:93], v[134:137], v[178:181], v[90:93]
	v_mfma_i32_16x16x64_i8 v[78:81], v[130:133], v[186:189], v[78:81]
	v_mfma_i32_16x16x64_i8 v[74:77], v[134:137], v[186:189], v[74:77]
	v_mfma_i32_16x16x64_i8 v[126:129], v[138:141], v[166:169], v[126:129]
	v_mfma_i32_16x16x64_i8 v[122:125], v[142:145], v[166:169], v[122:125]
	v_mfma_i32_16x16x64_i8 v[110:113], v[138:141], v[174:177], v[110:113]
	v_mfma_i32_16x16x64_i8 v[106:109], v[142:145], v[174:177], v[106:109]
	v_mfma_i32_16x16x64_i8 v[94:97], v[138:141], v[182:185], v[94:97]
	v_mfma_i32_16x16x64_i8 v[90:93], v[142:145], v[182:185], v[90:93]
	v_mfma_i32_16x16x64_i8 v[78:81], v[138:141], v[190:193], v[78:81]
	v_mfma_i32_16x16x64_i8 v[74:77], v[142:145], v[190:193], v[74:77]
	s_setprio 0
	s_setprio 1
	v_mfma_i32_16x16x64_i8 v[118:121], v[146:149], v[162:165], v[118:121]
	v_mfma_i32_16x16x64_i8 v[114:117], v[150:153], v[162:165], v[114:117]
	v_mfma_i32_16x16x64_i8 v[102:105], v[146:149], v[170:173], v[102:105]
	v_mfma_i32_16x16x64_i8 v[98:101], v[150:153], v[170:173], v[98:101]
	v_mfma_i32_16x16x64_i8 v[86:89], v[146:149], v[178:181], v[86:89]
	v_mfma_i32_16x16x64_i8 v[82:85], v[150:153], v[178:181], v[82:85]
	v_mfma_i32_16x16x64_i8 v[70:73], v[146:149], v[186:189], v[70:73]
	v_mfma_i32_16x16x64_i8 v[66:69], v[150:153], v[186:189], v[66:69]
	v_mfma_i32_16x16x64_i8 v[118:121], v[154:157], v[166:169], v[118:121]
	v_mfma_i32_16x16x64_i8 v[114:117], v[158:161], v[166:169], v[114:117]
	v_mfma_i32_16x16x64_i8 v[102:105], v[154:157], v[174:177], v[102:105]
	v_mfma_i32_16x16x64_i8 v[98:101], v[158:161], v[174:177], v[98:101]
	v_mfma_i32_16x16x64_i8 v[86:89], v[154:157], v[182:185], v[86:89]
	v_mfma_i32_16x16x64_i8 v[82:85], v[158:161], v[182:185], v[82:85]
	v_mfma_i32_16x16x64_i8 v[70:73], v[154:157], v[190:193], v[70:73]
	v_mfma_i32_16x16x64_i8 v[66:69], v[158:161], v[190:193], v[66:69]
	s_setprio 0
	s_barrier
	s_add_i32 s30, s37, s43
	v_lshl_add_u64 v[246:247], s[34:35], 0, v[200:201]
	s_mov_b32 m0, s30
	ds_read_b128 v[162:165], v233 offset:49152
	ds_read_b128 v[166:169], v233 offset:50176
	ds_read_b128 v[170:173], v233 offset:51200
	ds_read_b128 v[174:177], v233 offset:52224
	ds_read_b128 v[178:181], v233 offset:53248
	ds_read_b128 v[182:185], v233 offset:54272
	ds_read_b128 v[186:189], v233 offset:55296
	ds_read_b128 v[190:193], v233 offset:56320
	global_load_lds_dwordx4 v[246:247], off
	s_add_i32 m0, s30, 0x2000
	s_add_u32 s28, s28, 0x9000
	v_lshl_add_u64 v[246:247], s[34:35], 0, v[196:197]
	s_addc_u32 s29, s29, 0
	s_add_i32 s30, s71, s43
	global_load_lds_dwordx4 v[246:247], off
	v_lshl_add_u64 v[246:247], s[28:29], 0, v[200:201]
	s_mov_b32 m0, s30
	v_lshl_add_u64 v[242:243], v[242:243], 0, s[10:11]
	global_load_lds_dwordx4 v[246:247], off
	v_lshl_add_u64 v[246:247], s[28:29], 0, v[196:197]
	s_add_i32 m0, s30, 0x2000
	s_nop 0
	global_load_lds_dwordx4 v[246:247], off
	s_mov_b32 m0, s58
	s_nop 0
	global_load_lds_dwordx4 v[242:243], off
	v_lshl_add_u64 v[242:243], v[244:245], 0, s[10:11]
	s_mov_b32 m0, s59
	s_nop 0
	global_load_lds_dwordx4 v[242:243], off
	s_waitcnt vmcnt(8)
	s_waitcnt lgkmcnt(0)
	s_barrier
	s_setprio 1
	s_waitcnt lgkmcnt(0)
	v_mfma_i32_16x16x64_i8 v[62:65], v[130:133], v[162:165], v[62:65]
	v_mfma_i32_16x16x64_i8 v[58:61], v[134:137], v[162:165], v[58:61]
	v_mfma_i32_16x16x64_i8 v[46:49], v[130:133], v[170:173], v[46:49]
	v_mfma_i32_16x16x64_i8 v[42:45], v[134:137], v[170:173], v[42:45]
	v_mfma_i32_16x16x64_i8 v[30:33], v[130:133], v[178:181], v[30:33]
	v_mfma_i32_16x16x64_i8 v[26:29], v[134:137], v[178:181], v[26:29]
	v_mfma_i32_16x16x64_i8 v[14:17], v[130:133], v[186:189], v[14:17]
	v_mfma_i32_16x16x64_i8 v[10:13], v[134:137], v[186:189], v[10:13]
	v_mfma_i32_16x16x64_i8 v[62:65], v[138:141], v[166:169], v[62:65]
	v_mfma_i32_16x16x64_i8 v[58:61], v[142:145], v[166:169], v[58:61]
	v_mfma_i32_16x16x64_i8 v[46:49], v[138:141], v[174:177], v[46:49]
	v_mfma_i32_16x16x64_i8 v[42:45], v[142:145], v[174:177], v[42:45]
	v_mfma_i32_16x16x64_i8 v[30:33], v[138:141], v[182:185], v[30:33]
	v_mfma_i32_16x16x64_i8 v[26:29], v[142:145], v[182:185], v[26:29]
	v_mfma_i32_16x16x64_i8 v[14:17], v[138:141], v[190:193], v[14:17]
	v_mfma_i32_16x16x64_i8 v[10:13], v[142:145], v[190:193], v[10:13]
	s_setprio 0
	s_setprio 1
	v_mfma_i32_16x16x64_i8 v[54:57], v[146:149], v[162:165], v[54:57]
	v_mfma_i32_16x16x64_i8 v[50:53], v[150:153], v[162:165], v[50:53]
	v_mfma_i32_16x16x64_i8 v[38:41], v[146:149], v[170:173], v[38:41]
	v_mfma_i32_16x16x64_i8 v[34:37], v[150:153], v[170:173], v[34:37]
	v_mfma_i32_16x16x64_i8 v[22:25], v[146:149], v[178:181], v[22:25]
	v_mfma_i32_16x16x64_i8 v[18:21], v[150:153], v[178:181], v[18:21]
	v_mfma_i32_16x16x64_i8 v[6:9], v[146:149], v[186:189], v[6:9]
	v_mfma_i32_16x16x64_i8 v[2:5], v[150:153], v[186:189], v[2:5]
	v_mfma_i32_16x16x64_i8 v[54:57], v[154:157], v[166:169], v[54:57]
	v_mfma_i32_16x16x64_i8 v[50:53], v[158:161], v[166:169], v[50:53]
	v_mfma_i32_16x16x64_i8 v[38:41], v[154:157], v[174:177], v[38:41]
	v_mfma_i32_16x16x64_i8 v[34:37], v[158:161], v[174:177], v[34:37]
	v_mfma_i32_16x16x64_i8 v[22:25], v[154:157], v[182:185], v[22:25]
	v_mfma_i32_16x16x64_i8 v[18:21], v[158:161], v[182:185], v[18:21]
	v_mfma_i32_16x16x64_i8 v[6:9], v[154:157], v[190:193], v[6:9]
	v_mfma_i32_16x16x64_i8 v[2:5], v[158:161], v[190:193], v[2:5]
	s_setprio 0
	s_barrier
	s_add_u32 s69, s69, 0x10000
	s_addc_u32 s70, s70, 0
	s_add_u32 s4, s4, 0x100
	s_addc_u32 s5, s5, 0
	s_cmp_gt_u32 s68, 13
	s_mov_b32 s68, s36
	s_cbranch_scc1 .LBB0_3839

.LBB0_3897:
	s_cmp_lt_i32 s56, 17
	s_cselect_b64 s[0:1], -1, 0
	s_cmp_gt_i32 s57, 16
	s_cselect_b64 s[4:5], -1, 0
	s_and_b64 s[0:1], s[0:1], s[4:5]
	s_andn2_b64 vcc, exec, s[0:1]
	s_cbranch_vccnz .LBB0_4010
	s_waitcnt vmcnt(0)
	v_mov_b32_e32 v4, v0
	v_mov_b32_e32 v1, 0
	global_load_dword v16, v1, s[2:3] sc1
	s_movk_i32 s0, 0x88
	v_cmp_gt_i32_e32 vcc, s0, v4
	s_and_saveexec_b64 s[0:1], vcc
	s_cbranch_execz .LBB0_3901
	v_ashrrev_i32_e32 v5, 31, v4
	v_add_u32_e32 v1, 0xfffffe00, v4
	v_lshl_add_u64 v[2:3], v[4:5], 2, s[96:97]
	s_mov_b64 s[4:5], 0x504000
	v_lshl_add_u32 v4, v4, 2, 0
	v_lshl_add_u64 v[2:3], v[2:3], 0, s[4:5]
	v_add_u32_e32 v4, 0x20000, v4
	s_mov_b64 s[4:5], 0
	s_mov_b64 s[8:9], 0x800
	s_movk_i32 s10, 0xfe87

.LBB0_3901:
	s_or_b64 exec, exec, s[0:1]
	s_waitcnt vmcnt(0)
	v_readfirstlane_b32 s15, v16
	s_cmpk_lt_i32 s86, 0x400
	s_cselect_b64 s[0:1], -1, 0
	s_cmpk_gt_i32 s86, 0x3ff
	v_readfirstlane_b32 s12, v0
	s_waitcnt lgkmcnt(0)
	s_barrier
	s_cbranch_scc1 .LBB0_3904
	s_ashr_i32 s4, s86, 31
	s_lshr_b32 s4, s4, 29
	s_add_i32 s10, s86, s4
	s_and_b32 s4, s10, -8
	s_sub_i32 s8, s86, s4
	s_cmp_gt_i32 s8, -1
	s_cbranch_scc0 .LBB0_3905
	s_lshl_b32 s9, s8, 7
	s_ashr_i32 s4, s10, 3
	s_cbranch_execz .LBB0_3906
	s_branch .LBB0_3907

.LBB0_4010:
	s_cmp_lt_i32 s56, 18
	s_cselect_b64 s[0:1], -1, 0
	s_cmp_gt_i32 s57, 17
	s_cselect_b64 s[4:5], -1, 0
	s_and_b64 s[0:1], s[0:1], s[4:5]
	s_andn2_b64 vcc, exec, s[0:1]
	s_mov_b32 s13, 1
	s_cbranch_vccnz .LBB0_4074
	s_waitcnt vmcnt(0)
	v_mov_b32_e32 v1, 0
	global_load_dword v16, v1, s[2:3] sc1
	v_readlane_b32 s0, v254, 7
	s_lshl_b32 s0, s0, 3
	v_readlane_b32 s1, v254, 44
	s_add_i32 s20, s0, s1
	s_cmpk_lt_i32 s20, 0x4000
	s_cselect_b64 s[2:3], -1, 0
	s_cmpk_gt_i32 s20, 0x3fff
	s_mov_b64 s[22:23], 0
	s_cbranch_scc1 .LBB0_4015
	s_ashr_i32 s21, s20, 31
	s_lshl_b64 s[0:1], s[20:21], 3
	s_add_u32 s0, s49, s0
	s_addc_u32 s1, s50, s1
	v_mov_b32_e32 v1, 0
	global_load_dwordx2 v[2:3], v1, s[0:1] sc1
	s_waitcnt vmcnt(0)
	v_readfirstlane_b32 s22, v2
	v_readfirstlane_b32 s23, v3

.LBB0_4017:
	s_and_b64 vcc, exec, s[0:1]
	s_cbranch_vccnz .LBB0_4074
	s_waitcnt vmcnt(0)
	v_readfirstlane_b32 s0, v16
	s_lshl_b32 s0, s0, 3
	s_addk_i32 s0, 0xfc00
	s_cmp_lt_i32 s0, 1
	s_cbranch_scc1 .Lp17_s
	s_lshl_b32 s1, s0, 1
	s_cmp_gt_i32 s1, s94
	s_cselect_b32 s1, 1, 2
	s_lshl_b32 s2, s0, 2
	s_cmp_gt_i32 s2, s94
	s_mul_i32 s2, s0, 7
	s_cselect_b32 s1, s1, 4
	s_cmp_gt_i32 s2, s94
	s_mul_i32 s0, s0, 14
	s_cselect_b32 s1, s1, 7
	s_cmp_gt_i32 s0, s94
	s_cselect_b32 s13, s1, 14
.Lp17_s:
	s_lshl_b32 s4, s94, 3
	s_add_u32 s38, s96, 0x26a000
	s_addc_u32 s39, s97, 0
	s_add_u32 s6, s96, 0x64e00000
	s_addc_u32 s7, s97, 0
	s_add_u32 s40, s96, 0x60200000
	s_addc_u32 s41, s97, 0
	s_ashr_i32 s5, s4, 31
	s_lshl_b64 s[0:1], s[4:5], 3
	s_add_u32 s5, s33, s0
	s_addc_u32 s33, s48, s1
	v_and_b32_e32 v1, 63, v0
	s_add_u32 s42, s49, s0
	s_addc_u32 s43, s50, s1
	v_lshlrev_b32_e32 v26, 3, v1
	v_readlane_b32 s0, v255, 3
	v_bfe_u32 v27, v0, 5, 1
	v_and_b32_e32 v0, 0xf8, v26
	v_mov_b32_e32 v29, 0
	v_bfe_u32 v2, v1, 5, 24
	v_or_b32_e32 v30, 0x400, v26
	v_or_b32_e32 v32, 0x600, v26
	v_lshlrev_b32_e32 v28, 4, v1
	v_readlane_b32 s1, v255, 4
	s_lshl_b32 s44, s13, 18
	s_mov_b32 s8, 0
	v_or_b32_e32 v31, 2, v2
	v_lshrrev_b32_e32 v33, 8, v30
	v_lshrrev_b32_e32 v42, 8, v32
	v_lshl_add_u64 v[34:35], s[0:1], 0, v[28:29]
	v_lshl_add_u64 v[36:37], s[6:7], 0, v[28:29]
	s_mov_b64 s[10:11], 0x40000
	s_mov_b32 s12, 0x3b000000
	v_lshlrev_b32_e32 v38, 2, v0
	s_waitcnt vmcnt(0)
	v_mov_b64_e32 v[40:41], v[24:25]
	s_mov_b64 s[16:17], s[22:23]
	s_branch .LBB0_4020
